# layer-1 w_down fp8 conversion moved from the scan R2 phase to the layer-1 top-k phase (DN_R2 4096 -> 0)
# baseline (speedup 1.0000x reference)
.LBB0_1916:
	s_or_b64 exec, exec, s[0:1]
	s_movk_i32 s0, 0
	v_cmp_gt_i32_e32 vcc, s0, v24
	s_and_saveexec_b64 s[0:1], vcc
	s_cbranch_execz .LBB0_1919
	s_add_u32 s4, s48, 0x50000000
	s_addc_u32 s5, s49, 0
	s_mov_b64 s[6:7], 0
	s_mov_b32 s9, 0x2e8ba2e9
	s_mov_b32 s10, 0xb00000
	v_mov_b64_e32 v[22:23], s[74:75]
	v_mov_b32_e32 v21, 0
	v_add_u32_e32 v31, 0x410, v26
	v_add_u32_e32 v32, 0x418, v26
	v_add_u32_e32 v33, 0x820, v26
	v_add_u32_e32 v34, 0x828, v26
	v_add_u32_e32 v35, 0xc30, v26
	v_add_u32_e32 v36, 0xc38, v26
	v_add_u32_e32 v37, 0x1040, v26
	v_add_u32_e32 v38, 0x1048, v26
	v_add_u32_e32 v39, 0x1450, v26
	v_add_u32_e32 v40, 0x1458, v26
	v_add_u32_e32 v41, 0x1860, v26
	v_add_u32_e32 v42, 0x1868, v26
	v_add_u32_e32 v43, 0x1c70, v26
	v_add_u32_e32 v44, 0x1c78, v26
	v_add_u32_e32 v45, 0x2080, v26
	v_add_u32_e32 v46, 0x2088, v26
	v_add_u32_e32 v47, 0x2490, v26
	v_add_u32_e32 v48, 0x2498, v26
	v_add_u32_e32 v49, 0x28a0, v26
	v_add_u32_e32 v50, 0x28a8, v26
	v_add_u32_e32 v51, 0x2cb0, v26
	v_add_u32_e32 v52, 0x2cb8, v26
	v_add_u32_e32 v53, 0x30c0, v26
	v_add_u32_e32 v54, 0x30c8, v26
	v_add_u32_e32 v55, 0x34d0, v26
	v_add_u32_e32 v56, 0x34d8, v26
	v_add_u32_e32 v57, 0x38e0, v26
	v_add_u32_e32 v58, 0x38e8, v26
	v_add_u32_e32 v59, 0x3cf0, v26
	v_add_u32_e32 v60, 0x3cf8, v26
	s_mov_b32 s11, 0xc3e00000
	v_mov_b32_e32 v61, 0x43e00000
	s_movk_i32 s12, 0xfff
	v_mov_b32_e32 v62, 6
	v_add_u32_e32 v63, 0x400, v1
	v_add_u32_e32 v64, 0x800, v1
	v_add_u32_e32 v65, 0xc00, v1

.LBB0_2375:
	s_cmp_gt_i32 s50, 19
	s_cselect_b64 s[0:1], -1, 0
	s_cmp_lt_i32 s51, 20
	s_cselect_b64 s[2:3], -1, 0
	s_or_b64 s[2:3], s[0:1], s[2:3]
	s_and_b64 vcc, exec, s[2:3]
	s_cbranch_vccnz .LBB0_2592
	v_readlane_b32 s0, v253, 0
	v_readlane_b32 s1, v253, 1
	s_mov_b32 s4, s0
	s_cmp_lt_i32 s0, 32
	s_cselect_b64 s[0:1], -1, 0
	s_cmp_gt_i32 s4, 31
	v_readlane_b32 s6, v253, 63
	s_waitcnt vmcnt(0)
	v_ashrrev_i32_e32 v25, 6, v138
	s_cselect_b64 s[4:5], -1, 0
	s_addk_i32 s6, 0xff00
	v_add_u32_e32 v1, s6, v25
	s_movk_i32 s6, 0x2c00
	v_cmp_gt_i32_e32 vcc, s6, v1
	v_and_b32_e32 v24, 63, v138
	s_and_b64 s[6:7], s[4:5], vcc
	s_and_saveexec_b64 s[4:5], s[6:7]
	s_cbranch_execz .LBB0_2379
	s_movk_i32 s6, 0x4200
	v_mul_lo_u32 v2, v25, s6
	s_waitcnt lgkmcnt(0)
	v_add_u32_e32 v3, 0, v2
	v_lshlrev_b32_e32 v2, 2, v24
	v_lshlrev_b32_e32 v6, 4, v24
	v_lshrrev_b32_e32 v26, 4, v24
	v_and_b32_e32 v2, 60, v2
	v_and_b32_e32 v18, 48, v6
	s_add_i32 s10, s70, 0xffffff00
	v_lshl_add_u32 v4, v2, 2, v3
	v_mul_u32_u24_e32 v5, 0x104, v26
	v_mul_u32_u24_e32 v6, 0x104, v18
	v_and_b32_e32 v7, 60, v24
	s_add_u32 s6, s48, 0x50000000
	v_mov_b32_e32 v19, 0
	v_lshrrev_b32_e32 v27, 2, v24
	v_add3_u32 v28, v3, v6, v7
	v_add_u32_e32 v32, v4, v5
	s_addc_u32 s7, s49, 0
	v_or_b32_e32 v29, 16, v27
	v_or_b32_e32 v30, 32, v27
	v_or_b32_e32 v31, 48, v27
	s_mov_b64 s[8:9], 0
	s_mov_b32 s11, 0x2e8ba2e9
	s_mov_b32 s12, 0xb00000
	v_mov_b64_e32 v[20:21], s[74:75]
	v_lshlrev_b32_e32 v22, 2, v2
	v_mov_b32_e32 v23, v19
	v_add_u32_e32 v33, 0x410, v32
	v_add_u32_e32 v34, 0x418, v32
	v_add_u32_e32 v35, 0x820, v32
	v_add_u32_e32 v36, 0x828, v32
	v_add_u32_e32 v37, 0xc30, v32
	v_add_u32_e32 v38, 0xc38, v32
	v_add_u32_e32 v39, 0x1040, v32
	v_add_u32_e32 v40, 0x1048, v32
	v_add_u32_e32 v41, 0x1450, v32
	v_add_u32_e32 v42, 0x1458, v32
	v_add_u32_e32 v43, 0x1860, v32
	v_add_u32_e32 v44, 0x1868, v32
	v_add_u32_e32 v45, 0x1c70, v32
	v_add_u32_e32 v46, 0x1c78, v32
	v_add_u32_e32 v47, 0x2080, v32
	v_add_u32_e32 v48, 0x2088, v32
	v_add_u32_e32 v49, 0x2490, v32
	v_add_u32_e32 v50, 0x2498, v32
	v_add_u32_e32 v51, 0x28a0, v32
	v_add_u32_e32 v52, 0x28a8, v32
	v_add_u32_e32 v53, 0x2cb0, v32
	v_add_u32_e32 v54, 0x2cb8, v32
	v_add_u32_e32 v55, 0x30c0, v32
	v_add_u32_e32 v56, 0x30c8, v32
	v_add_u32_e32 v57, 0x34d0, v32
	v_add_u32_e32 v58, 0x34d8, v32
	v_add_u32_e32 v59, 0x38e0, v32
	v_add_u32_e32 v60, 0x38e8, v32
	v_add_u32_e32 v61, 0x3cf0, v32
	v_add_u32_e32 v62, 0x3cf8, v32
	s_mov_b32 s13, 0xc3e00000
	v_mov_b32_e32 v63, 0x43e00000
	s_movk_i32 s14, 0x2bff
	v_mov_b32_e32 v64, 6
	v_add_u32_e32 v65, 0x400, v28
	v_add_u32_e32 v66, 0x800, v28
	v_add_u32_e32 v67, 0xc00, v28
.LBB0_2378:
	v_mov_b32_e32 v70, v1
	v_mul_hi_i32 v68, v70, s11
	v_lshrrev_b32_e32 v69, 31, v68
	v_ashrrev_i32_e32 v68, 7, v68
	v_add_u32_e32 v68, v68, v69
	v_mul_i32_i24_e32 v72, 0x2c0, v68
	v_sub_u32_e32 v72, v70, v72
	v_ashrrev_i16_e32 v73, 15, v72
	v_lshrrev_b16_e32 v73, 12, v73
	v_add_u16_e32 v73, v72, v73
	v_ashrrev_i16_e32 v74, 4, v73
	v_and_b32_e32 v73, -16, v73
	v_sub_u16_e32 v73, v72, v73
	v_lshlrev_b32_sdwa v72, v64, sext(v74) dst_sel:DWORD dst_unused:UNUSED_PAD src0_sel:DWORD src1_sel:WORD_0
	v_add_u32_e32 v71, 16, v68
	v_lshlrev_b32_sdwa v74, v64, sext(v73) dst_sel:DWORD dst_unused:UNUSED_PAD src0_sel:DWORD src1_sel:WORD_0
	v_or_b32_e32 v76, v72, v26
	v_mul_hi_i32_i24_e32 v69, 0x2c0000, v68
	v_mul_i32_i24_e32 v68, 0x2c0000, v68
	v_mad_i64_i32 v[70:71], s[16:17], v71, s12, v[20:21]
	v_ashrrev_i32_e32 v75, 31, v74
	v_or_b32_e32 v78, 4, v76
	v_or_b32_e32 v80, 8, v76
	v_or_b32_e32 v82, 12, v76
	v_or_b32_e32 v84, 16, v76
	v_or_b32_e32 v86, 20, v76
	v_or_b32_e32 v88, 24, v76
	v_or_b32_e32 v90, 28, v76
	v_or_b32_e32 v92, 32, v76
	v_or_b32_e32 v94, 36, v76
	v_lshl_add_u64 v[68:69], s[6:7], 0, v[68:69]
	v_ashrrev_i32_e32 v73, 31, v72
	v_ashrrev_i32_e32 v77, 31, v76
	v_or_b32_e32 v96, 40, v76
	v_or_b32_e32 v98, 44, v76
	v_or_b32_e32 v100, 48, v76
	v_or_b32_e32 v102, 52, v76
	v_or_b32_e32 v104, 56, v76
	v_or_b32_e32 v106, 60, v76
	v_or_b32_e32 v108, v74, v27
	v_or_b32_e32 v109, v74, v29
	v_or_b32_e32 v110, v74, v30
	v_or_b32_e32 v111, v74, v31
	v_lshl_add_u64 v[70:71], v[74:75], 2, v[70:71]
	v_ashrrev_i32_e32 v79, 31, v78
	v_ashrrev_i32_e32 v81, 31, v80
	v_ashrrev_i32_e32 v83, 31, v82
	v_ashrrev_i32_e32 v85, 31, v84
	v_ashrrev_i32_e32 v87, 31, v86
	v_ashrrev_i32_e32 v89, 31, v88
	v_ashrrev_i32_e32 v91, 31, v90
	v_ashrrev_i32_e32 v93, 31, v92
	v_ashrrev_i32_e32 v95, 31, v94
	v_lshl_add_u64 v[68:69], v[68:69], 0, v[72:73]
	v_lshlrev_b64 v[72:73], 12, v[76:77]
	v_ashrrev_i32_e32 v97, 31, v96
	v_ashrrev_i32_e32 v99, 31, v98
	v_ashrrev_i32_e32 v101, 31, v100
	v_ashrrev_i32_e32 v103, 31, v102
	v_ashrrev_i32_e32 v105, 31, v104
	v_ashrrev_i32_e32 v107, 31, v106
	v_mul_i32_i24_e32 v74, 0xb00, v108
	v_mul_i32_i24_e32 v76, 0xb00, v109
	v_mul_i32_i24_e32 v108, 0xb00, v110
	v_mul_i32_i24_e32 v110, 0xb00, v111
	v_lshl_add_u64 v[70:71], v[70:71], 0, v[22:23]
	v_lshlrev_b64 v[78:79], 12, v[78:79]
	v_lshlrev_b64 v[80:81], 12, v[80:81]
	v_lshlrev_b64 v[82:83], 12, v[82:83]
	v_lshlrev_b64 v[84:85], 12, v[84:85]
	v_lshlrev_b64 v[86:87], 12, v[86:87]
	v_lshlrev_b64 v[88:89], 12, v[88:89]
	v_lshlrev_b64 v[90:91], 12, v[90:91]
	v_lshlrev_b64 v[92:93], 12, v[92:93]
	v_lshlrev_b64 v[94:95], 12, v[94:95]
	v_lshl_add_u64 v[68:69], v[68:69], 0, v[18:19]
	v_lshlrev_b64 v[96:97], 12, v[96:97]
	v_lshlrev_b64 v[98:99], 12, v[98:99]
	v_lshlrev_b64 v[100:101], 12, v[100:101]
	v_lshlrev_b64 v[102:103], 12, v[102:103]
	v_lshlrev_b64 v[104:105], 12, v[104:105]
	v_lshlrev_b64 v[106:107], 12, v[106:107]
	v_ashrrev_i32_e32 v75, 31, v74
	v_ashrrev_i32_e32 v77, 31, v76
	v_ashrrev_i32_e32 v109, 31, v108
	v_ashrrev_i32_e32 v111, 31, v110
	v_lshl_add_u64 v[112:113], v[70:71], 0, v[72:73]
	v_lshl_add_u64 v[114:115], v[70:71], 0, v[78:79]
	v_lshl_add_u64 v[116:117], v[70:71], 0, v[80:81]
	v_lshl_add_u64 v[118:119], v[70:71], 0, v[82:83]
	v_lshl_add_u64 v[120:121], v[70:71], 0, v[84:85]
	v_lshl_add_u64 v[122:123], v[70:71], 0, v[86:87]
	v_lshl_add_u64 v[124:125], v[70:71], 0, v[88:89]
	v_lshl_add_u64 v[126:127], v[70:71], 0, v[90:91]
	v_lshl_add_u64 v[128:129], v[70:71], 0, v[92:93]
	v_lshl_add_u64 v[130:131], v[70:71], 0, v[94:95]
	v_lshl_add_u64 v[132:133], v[70:71], 0, v[96:97]
	v_lshl_add_u64 v[134:135], v[70:71], 0, v[98:99]
	v_lshl_add_u64 v[136:137], v[70:71], 0, v[100:101]
	v_lshl_add_u64 v[140:141], v[70:71], 0, v[102:103]
	v_lshl_add_u64 v[142:143], v[70:71], 0, v[104:105]
	v_lshl_add_u64 v[144:145], v[70:71], 0, v[106:107]
	v_lshl_add_u64 v[146:147], v[68:69], 0, v[74:75]
	v_lshl_add_u64 v[148:149], v[68:69], 0, v[76:77]
	v_lshl_add_u64 v[150:151], v[68:69], 0, v[108:109]
	v_lshl_add_u64 v[152:153], v[68:69], 0, v[110:111]
	global_load_dwordx4 v[68:71], v[112:113], off nt
	global_load_dwordx4 v[72:75], v[114:115], off nt
	global_load_dwordx4 v[76:79], v[116:117], off nt
	global_load_dwordx4 v[80:83], v[118:119], off nt
	global_load_dwordx4 v[84:87], v[120:121], off nt
	global_load_dwordx4 v[88:91], v[122:123], off nt
	global_load_dwordx4 v[92:95], v[124:125], off nt
	global_load_dwordx4 v[96:99], v[126:127], off nt
	global_load_dwordx4 v[100:103], v[128:129], off nt
	global_load_dwordx4 v[104:107], v[130:131], off nt
	global_load_dwordx4 v[108:111], v[132:133], off nt
	global_load_dwordx4 v[112:115], v[134:135], off nt
	global_load_dwordx4 v[116:119], v[136:137], off nt
	global_load_dwordx4 v[120:123], v[140:141], off nt
	global_load_dwordx4 v[124:127], v[142:143], off nt
	global_load_dwordx4 v[128:131], v[144:145], off nt
	s_waitcnt vmcnt(15)
	ds_write2_b32 v32, v68, v69 offset1:1
	ds_write2_b32 v32, v70, v71 offset0:2 offset1:3
	s_waitcnt vmcnt(14)
	ds_write2_b32 v33, v72, v73 offset1:1
	ds_write2_b32 v34, v74, v75 offset1:1
	s_waitcnt vmcnt(13)
	ds_write2_b32 v35, v76, v77 offset1:1
	ds_write2_b32 v36, v78, v79 offset1:1
	s_waitcnt vmcnt(12)
	ds_write2_b32 v37, v80, v81 offset1:1
	ds_write2_b32 v38, v82, v83 offset1:1
	s_waitcnt vmcnt(11)
	ds_write2_b32 v39, v84, v85 offset1:1
	ds_write2_b32 v40, v86, v87 offset1:1
	s_waitcnt vmcnt(10)
	ds_write2_b32 v41, v88, v89 offset1:1
	ds_write2_b32 v42, v90, v91 offset1:1
	s_waitcnt vmcnt(9)
	ds_write2_b32 v43, v92, v93 offset1:1
	ds_write2_b32 v44, v94, v95 offset1:1
	s_waitcnt vmcnt(8)
	ds_write2_b32 v45, v96, v97 offset1:1
	ds_write2_b32 v46, v98, v99 offset1:1
	s_waitcnt vmcnt(7)
	ds_write2_b32 v47, v100, v101 offset1:1
	ds_write2_b32 v48, v102, v103 offset1:1
	s_waitcnt vmcnt(6)
	ds_write2_b32 v49, v104, v105 offset1:1
	ds_write2_b32 v50, v106, v107 offset1:1
	s_waitcnt vmcnt(5)
	ds_write2_b32 v51, v108, v109 offset1:1
	ds_write2_b32 v52, v110, v111 offset1:1
	s_waitcnt vmcnt(4)
	ds_write2_b32 v53, v112, v113 offset1:1
	ds_write2_b32 v54, v114, v115 offset1:1
	s_waitcnt vmcnt(3)
	ds_write2_b32 v55, v116, v117 offset1:1
	ds_write2_b32 v56, v118, v119 offset1:1
	s_waitcnt vmcnt(2)
	ds_write2_b32 v57, v120, v121 offset1:1
	ds_write2_b32 v58, v122, v123 offset1:1
	s_waitcnt vmcnt(1)
	ds_write2_b32 v59, v124, v125 offset1:1
	ds_write2_b32 v60, v126, v127 offset1:1
	s_waitcnt vmcnt(0)
	ds_write2_b32 v61, v128, v129 offset1:1
	ds_write2_b32 v62, v130, v131 offset1:1
	s_waitcnt lgkmcnt(0)
	ds_read2_b32 v[68:69], v28 offset1:16
	ds_read2_b32 v[70:71], v28 offset0:65 offset1:81
	ds_read2_b32 v[72:73], v28 offset0:130 offset1:146
	ds_read2_b32 v[74:75], v28 offset0:195 offset1:211
	ds_read2_b32 v[76:77], v65 offset0:4 offset1:20
	ds_read2_b32 v[78:79], v65 offset0:69 offset1:85
	ds_read2_b32 v[80:81], v65 offset0:134 offset1:150
	ds_read2_b32 v[82:83], v65 offset0:199 offset1:215
	ds_read2_b32 v[84:85], v66 offset0:8 offset1:24
	ds_read2_b32 v[86:87], v66 offset0:73 offset1:89
	ds_read2_b32 v[88:89], v66 offset0:138 offset1:154
	ds_read2_b32 v[90:91], v66 offset0:203 offset1:219
	ds_read2_b32 v[92:93], v67 offset0:12 offset1:28
	ds_read2_b32 v[94:95], v67 offset0:77 offset1:93
	ds_read2_b32 v[96:97], v67 offset0:142 offset1:158
	ds_read2_b32 v[98:99], v67 offset0:207 offset1:223
	ds_read2_b32 v[100:101], v28 offset0:32 offset1:48
	ds_read2_b32 v[102:103], v28 offset0:97 offset1:113
	ds_read2_b32 v[104:105], v28 offset0:162 offset1:178
	ds_read2_b32 v[106:107], v28 offset0:227 offset1:243
	ds_read2_b32 v[108:109], v65 offset0:36 offset1:52
	ds_read2_b32 v[110:111], v65 offset0:101 offset1:117
	ds_read2_b32 v[112:113], v65 offset0:166 offset1:182
	ds_read2_b32 v[114:115], v65 offset0:231 offset1:247
	ds_read2_b32 v[116:117], v66 offset0:40 offset1:56
	ds_read2_b32 v[118:119], v66 offset0:105 offset1:121
	ds_read2_b32 v[120:121], v66 offset0:170 offset1:186
	ds_read2_b32 v[122:123], v66 offset0:235 offset1:251
	ds_read2_b32 v[124:125], v67 offset0:44 offset1:60
	ds_read2_b32 v[126:127], v67 offset0:109 offset1:125
	ds_read2_b32 v[128:129], v67 offset0:174 offset1:190
	ds_read2_b32 v[130:131], v67 offset0:239 offset1:255
	s_waitcnt lgkmcnt(14)
	v_mul_f32_e32 v68, 0x43800000, v68
	v_mul_f32_e32 v70, 0x43800000, v70
	v_mul_f32_e32 v76, 0x43800000, v76
	v_mul_f32_e32 v78, 0x43800000, v78
	v_mul_f32_e32 v84, 0x43800000, v84
	v_mul_f32_e32 v86, 0x43800000, v86
	v_mul_f32_e32 v92, 0x43800000, v92
	v_mul_f32_e32 v94, 0x43800000, v94
	v_mov_b32_e32 v2, 0
	v_mov_b32_e32 v3, 0
	v_mov_b32_e32 v4, 0
	v_mov_b32_e32 v5, 0
	v_mul_f32_e32 v69, 0x43800000, v69
	v_mul_f32_e32 v71, 0x43800000, v71
	v_mul_f32_e32 v77, 0x43800000, v77
	v_mul_f32_e32 v79, 0x43800000, v79
	v_mul_f32_e32 v85, 0x43800000, v85
	v_mul_f32_e32 v87, 0x43800000, v87
	v_mul_f32_e32 v93, 0x43800000, v93
	v_mul_f32_e32 v95, 0x43800000, v95
	v_med3_f32 v68, v68, s13, v63
	v_med3_f32 v70, v70, s13, v63
	v_med3_f32 v76, v76, s13, v63
	v_med3_f32 v78, v78, s13, v63
	v_med3_f32 v84, v84, s13, v63
	v_med3_f32 v86, v86, s13, v63
	v_med3_f32 v92, v92, s13, v63
	v_med3_f32 v94, v94, s13, v63
	v_mov_b32_e32 v6, 0
	v_mov_b32_e32 v7, 0
	v_mov_b32_e32 v8, 0
	v_mov_b32_e32 v9, 0
	v_mul_f32_e32 v100, 0x43800000, v100
	v_mul_f32_e32 v102, 0x43800000, v102
	s_waitcnt lgkmcnt(11)
	v_mul_f32_e32 v108, 0x43800000, v108
	s_waitcnt lgkmcnt(10)
	v_mul_f32_e32 v110, 0x43800000, v110
	s_waitcnt lgkmcnt(7)
	v_mul_f32_e32 v116, 0x43800000, v116
	s_waitcnt lgkmcnt(6)
	v_mul_f32_e32 v118, 0x43800000, v118
	s_waitcnt lgkmcnt(3)
	v_mul_f32_e32 v124, 0x43800000, v124
	s_waitcnt lgkmcnt(2)
	v_mul_f32_e32 v126, 0x43800000, v126
	v_med3_f32 v69, v69, s13, v63
	v_med3_f32 v71, v71, s13, v63
	v_med3_f32 v77, v77, s13, v63
	v_med3_f32 v79, v79, s13, v63
	v_med3_f32 v85, v85, s13, v63
	v_med3_f32 v87, v87, s13, v63
	v_med3_f32 v93, v93, s13, v63
	v_med3_f32 v95, v95, s13, v63
	v_cvt_pk_fp8_f32 v2, v68, v70
	v_cvt_pk_fp8_f32 v3, v76, v78
	v_cvt_pk_fp8_f32 v4, v84, v86
	v_cvt_pk_fp8_f32 v5, v92, v94
	v_mov_b32_e32 v10, 0
	v_mov_b32_e32 v11, 0
	v_mov_b32_e32 v12, 0
	v_mov_b32_e32 v13, 0
	v_mul_f32_e32 v101, 0x43800000, v101
	v_mul_f32_e32 v103, 0x43800000, v103
	v_mul_f32_e32 v109, 0x43800000, v109
	v_mul_f32_e32 v111, 0x43800000, v111
	v_mul_f32_e32 v117, 0x43800000, v117
	v_mul_f32_e32 v119, 0x43800000, v119
	v_mul_f32_e32 v125, 0x43800000, v125
	v_mul_f32_e32 v127, 0x43800000, v127
	v_med3_f32 v100, v100, s13, v63
	v_med3_f32 v102, v102, s13, v63
	v_med3_f32 v108, v108, s13, v63
	v_med3_f32 v110, v110, s13, v63
	v_med3_f32 v116, v116, s13, v63
	v_med3_f32 v118, v118, s13, v63
	v_med3_f32 v124, v124, s13, v63
	v_med3_f32 v126, v126, s13, v63
	v_cvt_pk_fp8_f32 v6, v69, v71
	v_cvt_pk_fp8_f32 v7, v77, v79
	v_cvt_pk_fp8_f32 v8, v85, v87
	v_cvt_pk_fp8_f32 v9, v93, v95
	v_mov_b32_e32 v14, 0
	v_mov_b32_e32 v15, 0
	v_mov_b32_e32 v16, 0
	v_mov_b32_e32 v17, 0
	v_mul_f32_e32 v72, 0x43800000, v72
	v_mul_f32_e32 v74, 0x43800000, v74
	v_mul_f32_e32 v80, 0x43800000, v80
	v_mul_f32_e32 v82, 0x43800000, v82
	v_mul_f32_e32 v88, 0x43800000, v88
	v_mul_f32_e32 v90, 0x43800000, v90
	v_mul_f32_e32 v96, 0x43800000, v96
	v_mul_f32_e32 v98, 0x43800000, v98
	v_med3_f32 v101, v101, s13, v63
	v_med3_f32 v103, v103, s13, v63
	v_med3_f32 v109, v109, s13, v63
	v_med3_f32 v111, v111, s13, v63
	v_med3_f32 v117, v117, s13, v63
	v_med3_f32 v119, v119, s13, v63
	v_med3_f32 v125, v125, s13, v63
	v_med3_f32 v127, v127, s13, v63
	v_cvt_pk_fp8_f32 v10, v100, v102
	v_cvt_pk_fp8_f32 v11, v108, v110
	v_cvt_pk_fp8_f32 v12, v116, v118
	v_cvt_pk_fp8_f32 v13, v124, v126
	v_mul_f32_e32 v73, 0x43800000, v73
	v_mul_f32_e32 v75, 0x43800000, v75
	v_mul_f32_e32 v81, 0x43800000, v81
	v_mul_f32_e32 v83, 0x43800000, v83
	v_mul_f32_e32 v89, 0x43800000, v89
	v_mul_f32_e32 v91, 0x43800000, v91
	v_mul_f32_e32 v97, 0x43800000, v97
	v_mul_f32_e32 v99, 0x43800000, v99
	v_med3_f32 v72, v72, s13, v63
	v_med3_f32 v74, v74, s13, v63
	v_med3_f32 v80, v80, s13, v63
	v_med3_f32 v82, v82, s13, v63
	v_med3_f32 v88, v88, s13, v63
	v_med3_f32 v90, v90, s13, v63
	v_med3_f32 v96, v96, s13, v63
	v_med3_f32 v98, v98, s13, v63
	v_cvt_pk_fp8_f32 v14, v101, v103
	v_cvt_pk_fp8_f32 v15, v109, v111
	v_cvt_pk_fp8_f32 v16, v117, v119
	v_cvt_pk_fp8_f32 v17, v125, v127
	v_mul_f32_e32 v104, 0x43800000, v104
	v_mul_f32_e32 v106, 0x43800000, v106
	v_mul_f32_e32 v112, 0x43800000, v112
	v_mul_f32_e32 v114, 0x43800000, v114
	v_mul_f32_e32 v120, 0x43800000, v120
	v_mul_f32_e32 v122, 0x43800000, v122
	s_waitcnt lgkmcnt(1)
	v_mul_f32_e32 v128, 0x43800000, v128
	s_waitcnt lgkmcnt(0)
	v_mul_f32_e32 v130, 0x43800000, v130
	v_med3_f32 v73, v73, s13, v63
	v_med3_f32 v75, v75, s13, v63
	v_med3_f32 v81, v81, s13, v63
	v_med3_f32 v83, v83, s13, v63
	v_med3_f32 v89, v89, s13, v63
	v_med3_f32 v91, v91, s13, v63
	v_med3_f32 v97, v97, s13, v63
	v_med3_f32 v99, v99, s13, v63
	v_cvt_pk_fp8_f32 v2, v72, v74 op_sel:[0,0,1]
	v_cvt_pk_fp8_f32 v3, v80, v82 op_sel:[0,0,1]
	v_cvt_pk_fp8_f32 v4, v88, v90 op_sel:[0,0,1]
	v_cvt_pk_fp8_f32 v5, v96, v98 op_sel:[0,0,1]
	v_mul_f32_e32 v105, 0x43800000, v105
	v_mul_f32_e32 v107, 0x43800000, v107
	v_mul_f32_e32 v113, 0x43800000, v113
	v_mul_f32_e32 v115, 0x43800000, v115
	v_mul_f32_e32 v121, 0x43800000, v121
	v_mul_f32_e32 v123, 0x43800000, v123
	v_mul_f32_e32 v129, 0x43800000, v129
	v_mul_f32_e32 v131, 0x43800000, v131
	v_med3_f32 v104, v104, s13, v63
	v_med3_f32 v106, v106, s13, v63
	v_med3_f32 v112, v112, s13, v63
	v_med3_f32 v114, v114, s13, v63
	v_med3_f32 v120, v120, s13, v63
	v_med3_f32 v122, v122, s13, v63
	v_med3_f32 v128, v128, s13, v63
	v_med3_f32 v130, v130, s13, v63
	v_cvt_pk_fp8_f32 v6, v73, v75 op_sel:[0,0,1]
	v_cvt_pk_fp8_f32 v7, v81, v83 op_sel:[0,0,1]
	v_cvt_pk_fp8_f32 v8, v89, v91 op_sel:[0,0,1]
	v_cvt_pk_fp8_f32 v9, v97, v99 op_sel:[0,0,1]
	v_med3_f32 v105, v105, s13, v63
	v_med3_f32 v107, v107, s13, v63
	v_med3_f32 v113, v113, s13, v63
	v_med3_f32 v115, v115, s13, v63
	v_med3_f32 v121, v121, s13, v63
	v_med3_f32 v123, v123, s13, v63
	v_med3_f32 v129, v129, s13, v63
	v_med3_f32 v131, v131, s13, v63
	v_cvt_pk_fp8_f32 v10, v104, v106 op_sel:[0,0,1]
	v_cvt_pk_fp8_f32 v11, v112, v114 op_sel:[0,0,1]
	v_cvt_pk_fp8_f32 v12, v120, v122 op_sel:[0,0,1]
	v_cvt_pk_fp8_f32 v13, v128, v130 op_sel:[0,0,1]
	v_cvt_pk_fp8_f32 v14, v105, v107 op_sel:[0,0,1]
	v_cvt_pk_fp8_f32 v15, v113, v115 op_sel:[0,0,1]
	v_cvt_pk_fp8_f32 v16, v121, v123 op_sel:[0,0,1]
	v_cvt_pk_fp8_f32 v17, v129, v131 op_sel:[0,0,1]
	global_store_dwordx4 v[146:147], v[2:5], off
	global_store_dwordx4 v[148:149], v[6:9], off
	global_store_dwordx4 v[150:151], v[10:13], off
	global_store_dwordx4 v[152:153], v[14:17], off
	v_add_u32_e32 v1, s10, v1
	s_waitcnt lgkmcnt(0)
	v_cmp_lt_i32_e32 vcc, s14, v1
	s_or_b64 s[8:9], vcc, s[8:9]
	s_andn2_b64 exec, exec, s[8:9]
	s_cbranch_execnz .LBB0_2378
